# v5 + grid barrier: non-leader workgroups spin on the cross-XCD release generation directly instead of waiting for their XCD leader's local release (one memory hop less per barrier)
# speedup vs baseline: 1.0125x; 1.0125x over previous
.LBB0_128:
	v_readlane_b32 s4, v250, 48
	s_lshl_b32 s4, s4, 8
	v_readlane_b32 s6, v250, 46
	v_readlane_b32 s7, v250, 47
	s_add_u32 s4, s6, s4
	s_addc_u32 s5, s7, 0
	v_mov_b32_e32 v2, 0x1000
	v_mov_b32_e32 v4, 1
	global_atomic_add v4, v2, v4, s[4:5] offset:1024 sc0
	v_cvt_f32_u32_e32 v2, v3
	v_sub_u32_e32 v5, 0, v3
	v_rcp_iflag_f32_e32 v2, v2
	s_nop 0
	v_mul_f32_e32 v2, 0x4f7ffffe, v2
	v_cvt_u32_f32_e32 v2, v2
	v_mul_lo_u32 v5, v5, v2
	v_mul_hi_u32 v5, v2, v5
	v_add_u32_e32 v2, v2, v5
	s_waitcnt vmcnt(0)
	v_mul_hi_u32 v2, v4, v2
	v_mul_lo_u32 v5, v2, v3
	v_sub_u32_e32 v5, v4, v5
	v_add_u32_e32 v6, 1, v2
	v_cmp_ge_u32_e32 vcc, v5, v3
	v_add_u32_e32 v4, 1, v4
	s_nop 0
	v_cndmask_b32_e32 v2, v2, v6, vcc
	v_sub_u32_e32 v6, v5, v3
	v_cndmask_b32_e32 v5, v5, v6, vcc
	v_add_u32_e32 v6, 1, v2
	v_cmp_ge_u32_e32 vcc, v5, v3
	s_nop 1
	v_cndmask_b32_e32 v2, v2, v6, vcc
	v_mul_lo_u32 v5, v3, v2
	v_add_u32_e32 v3, v5, v3
	v_cmp_ne_u32_e32 vcc, v4, v3
	s_and_saveexec_b64 s[6:7], vcc
	s_xor_b64 s[6:7], exec, s[6:7]
	s_cbranch_execz .LBB0_142
	s_waitcnt lgkmcnt(0)
	v_mov_b32_e32 v1, 0x7500
	global_load_dword v1, v1, s[78:79] sc1
	s_add_u32 s12, s78, 0x7500
	s_addc_u32 s13, s79, 0
	s_waitcnt vmcnt(0)
	v_cmp_eq_u32_e32 vcc, v1, v2
	s_and_saveexec_b64 s[8:9], vcc
	s_cbranch_execz .LBB0_141
	s_add_u32 s10, s78, 0x4200
	s_addc_u32 s11, s79, 0
	s_mov_b32 s24, 1
	s_mov_b64 s[14:15], 0
	v_mov_b32_e32 v1, 0
	s_branch .LBB0_132

.LBB0_1097:
	v_readlane_b32 s4, v250, 48
	s_lshl_b32 s4, s4, 8
	v_readlane_b32 s8, v250, 46
	v_readlane_b32 s9, v250, 47
	s_add_u32 s4, s8, s4
	s_addc_u32 s5, s9, 0
	v_mov_b32_e32 v2, 0x1000
	v_mov_b32_e32 v4, 1
	global_atomic_add v4, v2, v4, s[4:5] offset:1024 sc0
	v_cvt_f32_u32_e32 v2, v3
	v_sub_u32_e32 v5, 0, v3
	v_rcp_iflag_f32_e32 v2, v2
	s_nop 0
	v_mul_f32_e32 v2, 0x4f7ffffe, v2
	v_cvt_u32_f32_e32 v2, v2
	v_mul_lo_u32 v5, v5, v2
	v_mul_hi_u32 v5, v2, v5
	v_add_u32_e32 v2, v2, v5
	s_waitcnt vmcnt(0)
	v_mul_hi_u32 v2, v4, v2
	v_mul_lo_u32 v5, v2, v3
	v_sub_u32_e32 v5, v4, v5
	v_add_u32_e32 v6, 1, v2
	v_cmp_ge_u32_e32 vcc, v5, v3
	v_add_u32_e32 v4, 1, v4
	s_nop 0
	v_cndmask_b32_e32 v2, v2, v6, vcc
	v_sub_u32_e32 v6, v5, v3
	v_cndmask_b32_e32 v5, v5, v6, vcc
	v_add_u32_e32 v6, 1, v2
	v_cmp_ge_u32_e32 vcc, v5, v3
	s_nop 1
	v_cndmask_b32_e32 v2, v2, v6, vcc
	v_mul_lo_u32 v5, v3, v2
	v_add_u32_e32 v3, v5, v3
	v_cmp_ne_u32_e32 vcc, v4, v3
	s_and_saveexec_b64 s[8:9], vcc
	s_xor_b64 s[8:9], exec, s[8:9]
	s_cbranch_execz .LBB0_1111
	s_waitcnt lgkmcnt(0)
	v_mov_b32_e32 v1, 0x7500
	global_load_dword v1, v1, s[78:79] sc1
	s_add_u32 s14, s78, 0x7500
	s_addc_u32 s15, s79, 0
	s_waitcnt vmcnt(0)
	v_cmp_eq_u32_e32 vcc, v1, v2
	s_and_saveexec_b64 s[10:11], vcc
	s_cbranch_execz .LBB0_1110
	s_add_u32 s12, s78, 0x4200
	s_addc_u32 s13, s79, 0
	s_mov_b32 s28, 1
	s_mov_b64 s[16:17], 0
	v_mov_b32_e32 v1, 0
	s_branch .LBB0_1101

.LBB0_1152:
	v_readlane_b32 s2, v250, 48
	s_lshl_b32 s2, s2, 8
	v_readlane_b32 s4, v250, 46
	v_readlane_b32 s5, v250, 47
	s_add_u32 s2, s4, s2
	s_addc_u32 s3, s5, 0
	v_mov_b32_e32 v2, 0x1000
	v_mov_b32_e32 v4, 1
	global_atomic_add v4, v2, v4, s[2:3] offset:1024 sc0
	v_cvt_f32_u32_e32 v2, v3
	v_sub_u32_e32 v5, 0, v3
	v_rcp_iflag_f32_e32 v2, v2
	s_nop 0
	v_mul_f32_e32 v2, 0x4f7ffffe, v2
	v_cvt_u32_f32_e32 v2, v2
	v_mul_lo_u32 v5, v5, v2
	v_mul_hi_u32 v5, v2, v5
	v_add_u32_e32 v2, v2, v5
	s_waitcnt vmcnt(0)
	v_mul_hi_u32 v2, v4, v2
	v_mul_lo_u32 v5, v2, v3
	v_sub_u32_e32 v5, v4, v5
	v_add_u32_e32 v6, 1, v2
	v_cmp_ge_u32_e32 vcc, v5, v3
	v_add_u32_e32 v4, 1, v4
	s_nop 0
	v_cndmask_b32_e32 v2, v2, v6, vcc
	v_sub_u32_e32 v6, v5, v3
	v_cndmask_b32_e32 v5, v5, v6, vcc
	v_add_u32_e32 v6, 1, v2
	v_cmp_ge_u32_e32 vcc, v5, v3
	s_nop 1
	v_cndmask_b32_e32 v2, v2, v6, vcc
	v_mul_lo_u32 v5, v3, v2
	v_add_u32_e32 v3, v5, v3
	v_cmp_ne_u32_e32 vcc, v4, v3
	s_and_saveexec_b64 s[4:5], vcc
	s_xor_b64 s[4:5], exec, s[4:5]
	s_cbranch_execz .LBB0_1166
	s_waitcnt lgkmcnt(0)
	v_mov_b32_e32 v1, 0x7500
	global_load_dword v1, v1, s[78:79] sc1
	s_add_u32 s10, s78, 0x7500
	s_addc_u32 s11, s79, 0
	s_waitcnt vmcnt(0)
	v_cmp_eq_u32_e32 vcc, v1, v2
	s_and_saveexec_b64 s[6:7], vcc
	s_cbranch_execz .LBB0_1165
	s_add_u32 s8, s78, 0x4200
	s_addc_u32 s9, s79, 0
	s_mov_b32 s24, 1
	s_mov_b64 s[12:13], 0
	v_mov_b32_e32 v1, 0
	s_branch .LBB0_1156

.LBB0_1265:
	v_readlane_b32 s4, v250, 48
	s_lshl_b32 s4, s4, 8
	v_readlane_b32 s6, v250, 46
	v_readlane_b32 s7, v250, 47
	s_add_u32 s4, s6, s4
	s_addc_u32 s5, s7, 0
	v_mov_b32_e32 v2, 0x1000
	v_mov_b32_e32 v4, 1
	global_atomic_add v4, v2, v4, s[4:5] offset:1024 sc0
	v_cvt_f32_u32_e32 v2, v3
	v_sub_u32_e32 v5, 0, v3
	v_rcp_iflag_f32_e32 v2, v2
	s_nop 0
	v_mul_f32_e32 v2, 0x4f7ffffe, v2
	v_cvt_u32_f32_e32 v2, v2
	v_mul_lo_u32 v5, v5, v2
	v_mul_hi_u32 v5, v2, v5
	v_add_u32_e32 v2, v2, v5
	s_waitcnt vmcnt(0)
	v_mul_hi_u32 v2, v4, v2
	v_mul_lo_u32 v5, v2, v3
	v_sub_u32_e32 v5, v4, v5
	v_add_u32_e32 v6, 1, v2
	v_cmp_ge_u32_e32 vcc, v5, v3
	v_add_u32_e32 v4, 1, v4
	s_nop 0
	v_cndmask_b32_e32 v2, v2, v6, vcc
	v_sub_u32_e32 v6, v5, v3
	v_cndmask_b32_e32 v5, v5, v6, vcc
	v_add_u32_e32 v6, 1, v2
	v_cmp_ge_u32_e32 vcc, v5, v3
	s_nop 1
	v_cndmask_b32_e32 v2, v2, v6, vcc
	v_mul_lo_u32 v5, v3, v2
	v_add_u32_e32 v3, v5, v3
	v_cmp_ne_u32_e32 vcc, v4, v3
	s_and_saveexec_b64 s[6:7], vcc
	s_xor_b64 s[6:7], exec, s[6:7]
	s_cbranch_execz .LBB0_1279
	s_waitcnt lgkmcnt(0)
	v_mov_b32_e32 v1, 0x7500
	global_load_dword v1, v1, s[78:79] sc1
	s_add_u32 s12, s78, 0x7500
	s_addc_u32 s13, s79, 0
	s_waitcnt vmcnt(0)
	v_cmp_eq_u32_e32 vcc, v1, v2
	s_and_saveexec_b64 s[8:9], vcc
	s_cbranch_execz .LBB0_1278
	s_add_u32 s10, s78, 0x4200
	s_addc_u32 s11, s79, 0
	s_mov_b32 s26, 1
	s_mov_b64 s[14:15], 0
	v_mov_b32_e32 v1, 0
	s_branch .LBB0_1269

.LBB0_1430:
	v_readlane_b32 s6, v250, 48
	s_lshl_b32 s6, s6, 8
	v_readlane_b32 s8, v250, 46
	v_readlane_b32 s9, v250, 47
	s_add_u32 s6, s8, s6
	s_addc_u32 s7, s9, 0
	v_mov_b32_e32 v2, 0x1000
	v_mov_b32_e32 v4, 1
	global_atomic_add v4, v2, v4, s[6:7] offset:1024 sc0
	v_cvt_f32_u32_e32 v2, v3
	v_sub_u32_e32 v5, 0, v3
	v_rcp_iflag_f32_e32 v2, v2
	s_nop 0
	v_mul_f32_e32 v2, 0x4f7ffffe, v2
	v_cvt_u32_f32_e32 v2, v2
	v_mul_lo_u32 v5, v5, v2
	v_mul_hi_u32 v5, v2, v5
	v_add_u32_e32 v2, v2, v5
	s_waitcnt vmcnt(0)
	v_mul_hi_u32 v2, v4, v2
	v_mul_lo_u32 v5, v2, v3
	v_sub_u32_e32 v5, v4, v5
	v_add_u32_e32 v6, 1, v2
	v_cmp_ge_u32_e32 vcc, v5, v3
	v_add_u32_e32 v4, 1, v4
	s_nop 0
	v_cndmask_b32_e32 v2, v2, v6, vcc
	v_sub_u32_e32 v6, v5, v3
	v_cndmask_b32_e32 v5, v5, v6, vcc
	v_add_u32_e32 v6, 1, v2
	v_cmp_ge_u32_e32 vcc, v5, v3
	s_nop 1
	v_cndmask_b32_e32 v2, v2, v6, vcc
	v_mul_lo_u32 v5, v3, v2
	v_add_u32_e32 v3, v5, v3
	v_cmp_ne_u32_e32 vcc, v4, v3
	s_and_saveexec_b64 s[8:9], vcc
	s_xor_b64 s[8:9], exec, s[8:9]
	s_cbranch_execz .LBB0_1444
	s_waitcnt lgkmcnt(0)
	v_mov_b32_e32 v1, 0x7500
	global_load_dword v1, v1, s[78:79] sc1
	s_add_u32 s14, s78, 0x7500
	s_addc_u32 s15, s79, 0
	s_waitcnt vmcnt(0)
	v_cmp_eq_u32_e32 vcc, v1, v2
	s_and_saveexec_b64 s[10:11], vcc
	s_cbranch_execz .LBB0_1443
	s_add_u32 s12, s78, 0x4200
	s_addc_u32 s13, s79, 0
	s_mov_b32 s28, 1
	s_mov_b64 s[16:17], 0
	v_mov_b32_e32 v1, 0
	s_branch .LBB0_1434

.LBB0_1829:
	v_readlane_b32 s4, v250, 48
	s_lshl_b32 s4, s4, 8
	v_readlane_b32 s6, v250, 46
	v_readlane_b32 s7, v250, 47
	s_add_u32 s4, s6, s4
	s_addc_u32 s5, s7, 0
	v_mov_b32_e32 v1, 0x1000
	v_mov_b32_e32 v3, 1
	global_atomic_add v3, v1, v3, s[4:5] offset:1024 sc0
	v_cvt_f32_u32_e32 v1, v2
	v_sub_u32_e32 v4, 0, v2
	v_rcp_iflag_f32_e32 v1, v1
	s_nop 0
	v_mul_f32_e32 v1, 0x4f7ffffe, v1
	v_cvt_u32_f32_e32 v1, v1
	v_mul_lo_u32 v4, v4, v1
	v_mul_hi_u32 v4, v1, v4
	v_add_u32_e32 v1, v1, v4
	s_waitcnt vmcnt(0)
	v_mul_hi_u32 v1, v3, v1
	v_mul_lo_u32 v4, v1, v2
	v_sub_u32_e32 v4, v3, v4
	v_add_u32_e32 v5, 1, v1
	v_cmp_ge_u32_e32 vcc, v4, v2
	v_add_u32_e32 v3, 1, v3
	s_nop 0
	v_cndmask_b32_e32 v1, v1, v5, vcc
	v_sub_u32_e32 v5, v4, v2
	v_cndmask_b32_e32 v4, v4, v5, vcc
	v_add_u32_e32 v5, 1, v1
	v_cmp_ge_u32_e32 vcc, v4, v2
	s_nop 1
	v_cndmask_b32_e32 v1, v1, v5, vcc
	v_mul_lo_u32 v4, v2, v1
	v_add_u32_e32 v2, v4, v2
	v_cmp_ne_u32_e32 vcc, v3, v2
	s_and_saveexec_b64 s[6:7], vcc
	s_xor_b64 s[6:7], exec, s[6:7]
	s_cbranch_execz .LBB0_1843
	s_waitcnt lgkmcnt(0)
	v_mov_b32_e32 v0, 0x7500
	global_load_dword v0, v0, s[78:79] sc1
	s_add_u32 s12, s78, 0x7500
	s_addc_u32 s13, s79, 0
	s_waitcnt vmcnt(0)
	v_cmp_eq_u32_e32 vcc, v0, v1
	s_and_saveexec_b64 s[8:9], vcc
	s_cbranch_execz .LBB0_1842
	s_add_u32 s10, s78, 0x4200
	s_addc_u32 s11, s79, 0
	s_mov_b32 s24, 1
	s_mov_b64 s[14:15], 0
	v_mov_b32_e32 v0, 0
	s_branch .LBB0_1833
